# baseline (speedup 1.0000x reference)
.LBB0_5:
	v_add_u32_e32 v2, 0xffffff00, v0
	v_ashrrev_i32_e32 v2, 2, v2
	v_lshlrev_b32_e32 v1, 7, v1
	v_mad_i32_i24 v3, v2, s3, v1
	v_or_b32_e32 v8, 0x10c00, v1
	v_or_b32_e32 v12, 0x10e00, v1
	ds_read_b128 v[40:43], v3
	ds_read_b128 v[72:75], v8
	ds_read_b128 v[104:107], v12
	ds_read_b128 v[44:47], v3 offset:16
	ds_read_b128 v[76:79], v8 offset:16
	ds_read_b128 v[108:111], v12 offset:16
	ds_read_b128 v[48:51], v3 offset:32
	ds_read_b128 v[80:83], v8 offset:32
	ds_read_b128 v[112:115], v12 offset:32
	ds_read_b128 v[52:55], v3 offset:48
	ds_read_b128 v[84:87], v8 offset:48
	ds_read_b128 v[116:119], v12 offset:48
	ds_read_b128 v[56:59], v3 offset:64
	ds_read_b128 v[88:91], v8 offset:64
	ds_read_b128 v[120:123], v12 offset:64
	s_waitcnt lgkmcnt(12)
	v_fma_f32 v16, v40, v72, 0
	v_fma_f32 v17, v40, v104, 0
	v_fmac_f32_e32 v16, v41, v73
	v_fmac_f32_e32 v17, v41, v105
	v_fmac_f32_e32 v16, v42, v74
	v_fmac_f32_e32 v17, v42, v106
	v_fmac_f32_e32 v16, v43, v75
	v_fmac_f32_e32 v17, v43, v107
	ds_read_b128 v[60:63], v3 offset:80
	ds_read_b128 v[92:95], v8 offset:80
	ds_read_b128 v[124:127], v12 offset:80
	s_waitcnt lgkmcnt(12)
	v_fmac_f32_e32 v16, v44, v76
	v_fmac_f32_e32 v17, v44, v108
	v_fmac_f32_e32 v16, v45, v77
	v_fmac_f32_e32 v17, v45, v109
	v_fmac_f32_e32 v16, v46, v78
	v_fmac_f32_e32 v17, v46, v110
	v_fmac_f32_e32 v16, v47, v79
	v_fmac_f32_e32 v17, v47, v111
	ds_read_b128 v[64:67], v3 offset:96
	ds_read_b128 v[96:99], v8 offset:96
	ds_read_b128 v[128:131], v12 offset:96
	s_waitcnt lgkmcnt(12)
	v_fmac_f32_e32 v16, v48, v80
	v_fmac_f32_e32 v17, v48, v112
	v_fmac_f32_e32 v16, v49, v81
	v_fmac_f32_e32 v17, v49, v113
	v_fmac_f32_e32 v16, v50, v82
	v_fmac_f32_e32 v17, v50, v114
	v_fmac_f32_e32 v16, v51, v83
	v_fmac_f32_e32 v17, v51, v115
	ds_read_b128 v[68:71], v3 offset:112
	ds_read_b128 v[100:103], v8 offset:112
	ds_read_b128 v[132:135], v12 offset:112
	s_waitcnt lgkmcnt(12)
	v_fmac_f32_e32 v16, v52, v84
	v_fmac_f32_e32 v17, v52, v116
	v_fmac_f32_e32 v16, v53, v85
	v_fmac_f32_e32 v17, v53, v117
	v_fmac_f32_e32 v16, v54, v86
	v_fmac_f32_e32 v17, v54, v118
	v_fmac_f32_e32 v16, v55, v87
	v_fmac_f32_e32 v17, v55, v119
	s_waitcnt lgkmcnt(9)
	v_fmac_f32_e32 v16, v56, v88
	v_fmac_f32_e32 v17, v56, v120
	v_fmac_f32_e32 v16, v57, v89
	v_fmac_f32_e32 v17, v57, v121
	v_fmac_f32_e32 v16, v58, v90
	v_fmac_f32_e32 v17, v58, v122
	v_fmac_f32_e32 v16, v59, v91
	v_fmac_f32_e32 v17, v59, v123
	s_waitcnt lgkmcnt(6)
	v_fmac_f32_e32 v16, v60, v92
	v_fmac_f32_e32 v17, v60, v124
	v_fmac_f32_e32 v16, v61, v93
	v_fmac_f32_e32 v17, v61, v125
	v_fmac_f32_e32 v16, v62, v94
	v_fmac_f32_e32 v17, v62, v126
	v_fmac_f32_e32 v16, v63, v95
	v_fmac_f32_e32 v17, v63, v127
	s_waitcnt lgkmcnt(3)
	v_fmac_f32_e32 v16, v64, v96
	v_fmac_f32_e32 v17, v64, v128
	v_fmac_f32_e32 v16, v65, v97
	v_fmac_f32_e32 v17, v65, v129
	v_fmac_f32_e32 v16, v66, v98
	v_fmac_f32_e32 v17, v66, v130
	v_fmac_f32_e32 v16, v67, v99
	v_fmac_f32_e32 v17, v67, v131
	s_waitcnt lgkmcnt(0)
	v_fmac_f32_e32 v16, v68, v100
	v_fmac_f32_e32 v17, v68, v132
	v_fmac_f32_e32 v16, v69, v101
	v_fmac_f32_e32 v17, v69, v133
	v_fmac_f32_e32 v16, v70, v102
	v_fmac_f32_e32 v17, v70, v134
	v_fmac_f32_e32 v16, v71, v103
	v_fmac_f32_e32 v17, v71, v135
	ds_bpermute_b32 v1, v18, v16
	ds_bpermute_b32 v3, v18, v17
	s_waitcnt lgkmcnt(1)
	v_add_f32_e32 v1, v16, v1
	s_waitcnt lgkmcnt(0)
	v_add_f32_e32 v3, v17, v3
	ds_bpermute_b32 v4, v19, v1
	ds_bpermute_b32 v5, v19, v3
	s_and_saveexec_b64 s[4:5], vcc
	s_cbranch_execz .LBB0_7
	s_load_dwordx4 s[8:11], s[0:1], 0x20
	v_add_u32_e32 v2, s2, v2
	s_waitcnt lgkmcnt(0)
	v_add_f32_e32 v6, v3, v5
	v_ashrrev_i32_e32 v3, 31, v2
	v_add_f32_e32 v1, v1, v4
	v_lshlrev_b64 v[2:3], 2, v[2:3]
	v_mul_f32_e32 v1, 0x3fb8aa3b, v1
	v_lshl_add_u64 v[4:5], s[8:9], 0, v[2:3]
	global_store_dword v[4:5], v1, off
	v_mul_f32_e32 v1, 0x3fb8aa3b, v6
	v_lshl_add_u64 v[2:3], s[10:11], 0, v[2:3]
	global_store_dword v[2:3], v1, off

	.amdhsa_kernel _Z7gat_prePKfS0_S0_PDF16_PfS2_
		.amdhsa_group_segment_fixed_size 69632
		.amdhsa_private_segment_fixed_size 0
		.amdhsa_kernarg_size 48
		.amdhsa_user_sgpr_count 2
		.amdhsa_user_sgpr_dispatch_ptr 0
		.amdhsa_user_sgpr_queue_ptr 0
		.amdhsa_user_sgpr_kernarg_segment_ptr 1
		.amdhsa_user_sgpr_dispatch_id 0
		.amdhsa_user_sgpr_kernarg_preload_length 0
		.amdhsa_user_sgpr_kernarg_preload_offset 0
		.amdhsa_user_sgpr_private_segment_size 0
		.amdhsa_uses_dynamic_stack 0
		.amdhsa_enable_private_segment 0
		.amdhsa_system_sgpr_workgroup_id_x 1
		.amdhsa_system_sgpr_workgroup_id_y 0
		.amdhsa_system_sgpr_workgroup_id_z 0
		.amdhsa_system_sgpr_workgroup_info 0
		.amdhsa_system_vgpr_workitem_id 0
		.amdhsa_next_free_vgpr 136
		.amdhsa_next_free_sgpr 96
		.amdhsa_accum_offset 136
		.amdhsa_reserve_vcc 1
		.amdhsa_float_round_mode_32 0
		.amdhsa_float_round_mode_16_64 0
		.amdhsa_float_denorm_mode_32 3
		.amdhsa_float_denorm_mode_16_64 3
		.amdhsa_dx10_clamp 1
		.amdhsa_ieee_mode 1
		.amdhsa_fp16_overflow 0
		.amdhsa_tg_split 0
		.amdhsa_exception_fp_ieee_invalid_op 0
		.amdhsa_exception_fp_denorm_src 0
		.amdhsa_exception_fp_ieee_div_zero 0
		.amdhsa_exception_fp_ieee_overflow 0
		.amdhsa_exception_fp_ieee_underflow 0
		.amdhsa_exception_fp_ieee_inexact 0
		.amdhsa_exception_int_div_zero 0
	.end_amdhsa_kernel

.Lfunc_end0:
	.size	_Z7gat_prePKfS0_S0_PDF16_PfS2_, .Lfunc_end0-_Z7gat_prePKfS0_S0_PDF16_PfS2_
	.set _Z7gat_prePKfS0_S0_PDF16_PfS2_.num_vgpr, 136
	.set _Z7gat_prePKfS0_S0_PDF16_PfS2_.num_agpr, 0
	.set _Z7gat_prePKfS0_S0_PDF16_PfS2_.numbered_sgpr, 12
	.set _Z7gat_prePKfS0_S0_PDF16_PfS2_.num_named_barrier, 0
	.set _Z7gat_prePKfS0_S0_PDF16_PfS2_.private_seg_size, 0
	.set _Z7gat_prePKfS0_S0_PDF16_PfS2_.uses_vcc, 1
	.set _Z7gat_prePKfS0_S0_PDF16_PfS2_.uses_flat_scratch, 0
	.set _Z7gat_prePKfS0_S0_PDF16_PfS2_.has_dyn_sized_stack, 0
	.set _Z7gat_prePKfS0_S0_PDF16_PfS2_.has_recursion, 0
	.set _Z7gat_prePKfS0_S0_PDF16_PfS2_.has_indirect_call, 0

amdhsa.kernels:
  - .agpr_count:     0
    .args:
      - .actual_access:  read_only
        .address_space:  global
        .offset:         0
        .size:           8
        .value_kind:     global_buffer
      - .actual_access:  read_only
        .address_space:  global
        .offset:         8
        .size:           8
        .value_kind:     global_buffer
      - .actual_access:  read_only
        .address_space:  global
        .offset:         16
        .size:           8
        .value_kind:     global_buffer
      - .actual_access:  write_only
        .address_space:  global
        .offset:         24
        .size:           8
        .value_kind:     global_buffer
      - .actual_access:  write_only
        .address_space:  global
        .offset:         32
        .size:           8
        .value_kind:     global_buffer
      - .actual_access:  write_only
        .address_space:  global
        .offset:         40
        .size:           8
        .value_kind:     global_buffer
    .group_segment_fixed_size: 69632
    .kernarg_segment_align: 8
    .kernarg_segment_size: 48
    .language:       OpenCL C
    .language_version:
      - 2
      - 0
    .max_flat_workgroup_size: 512
    .name:           _Z7gat_prePKfS0_S0_PDF16_PfS2_
    .private_segment_fixed_size: 0
    .sgpr_count:     18
    .sgpr_spill_count: 0
    .symbol:         _Z7gat_prePKfS0_S0_PDF16_PfS2_.kd
    .uniform_work_group_size: 1
    .uses_dynamic_stack: false
    .vgpr_count:     136
    .vgpr_spill_count: 0
    .wavefront_size: 64
  - .agpr_count:     0
    .args:
      - .actual_access:  read_only
        .address_space:  global
        .offset:         0
        .size:           8
        .value_kind:     global_buffer
      - .actual_access:  read_only
        .address_space:  global
        .offset:         8
        .size:           8
        .value_kind:     global_buffer
      - .actual_access:  read_only
        .address_space:  global
        .offset:         16
        .size:           8
        .value_kind:     global_buffer
      - .actual_access:  read_only
        .address_space:  global
        .offset:         24
        .size:           8
        .value_kind:     global_buffer
      - .actual_access:  write_only
        .address_space:  global
        .offset:         32
        .size:           8
        .value_kind:     global_buffer
    .group_segment_fixed_size: 149536
    .kernarg_segment_align: 8
    .kernarg_segment_size: 40
    .language:       OpenCL C
    .language_version:
      - 2
      - 0
    .max_flat_workgroup_size: 512
    .name:           _Z8gat_mainPKiPKDF16_PKfS4_Pf
    .private_segment_fixed_size: 0
    .sgpr_count:     84
    .sgpr_spill_count: 0
    .symbol:         _Z8gat_mainPKiPKDF16_PKfS4_Pf.kd
    .uniform_work_group_size: 1
    .uses_dynamic_stack: false
    .vgpr_count:     232
    .vgpr_spill_count: 0
    .wavefront_size: 64
